# on top of the previous stack: map-1 waves pre-issue the first four K-fragment LDS reads of QK at the head of their P.V block
# baseline (speedup 1.0000x reference)
.LBB0_640:
	s_cmp_lg_u32 s42, 0
	s_barrier
	s_cselect_b64 s[62:63], -1, 0
	s_and_b64 s[0:1], s[56:57], s[62:63]
	s_andn2_b64 vcc, exec, s[0:1]
	s_cbranch_vccnz .LBB0_642
	s_add_i32 s0, s4, 0x8000
	s_and_b32 s0, s0, 0x18000
	v_add_u32_e32 v1, s0, v222
	s_add_i32 s0, s4, 0xffff0000
	s_and_b32 s0, s0, 0x18000
	v_add_u32_e32 v239, s0, v185
	v_add_u32_e32 v240, v239, v234
	ds_read_b128 v[148:151], v240
	ds_read_b128 v[152:155], v240 offset:8192
	v_add_u32_e32 v240, v239, v235
	ds_read_b128 v[156:159], v240
	ds_read_b128 v[160:163], v240 offset:8192
	s_waitcnt lgkmcnt(8)
	s_nop 0
	v_mfma_f32_32x32x16_bf16 v[52:67], v[96:99], v[100:103], v[52:67]
	v_mfma_f32_32x32x16_bf16 v[52:67], v[92:95], v[104:107], v[52:67]
	v_mfma_f32_32x32x16_bf16 v[52:67], v[88:91], v[108:111], v[52:67]
	v_mfma_f32_32x32x16_bf16 v[52:67], v[84:87], v[112:115], v[52:67]
	ds_read_b64_tr_b16 v[100:101], v1 offset:0x400
	ds_read_b64_tr_b16 v[102:103], v1 offset:0xc00
	ds_read_b64_tr_b16 v[104:105], v1 offset:0x1400
	ds_read_b64_tr_b16 v[106:107], v1 offset:0x1c00
	ds_read_b64_tr_b16 v[108:109], v1 offset:0x2400
	ds_read_b64_tr_b16 v[110:111], v1 offset:0x2c00
	ds_read_b64_tr_b16 v[112:113], v1 offset:0x3400
	ds_read_b64_tr_b16 v[114:115], v1 offset:0x3c00
	s_waitcnt lgkmcnt(8)
	v_mfma_f32_32x32x16_bf16 v[36:51], v[96:99], v[116:119], v[36:51]
	v_mfma_f32_32x32x16_bf16 v[36:51], v[92:95], v[120:123], v[36:51]
	v_mfma_f32_32x32x16_bf16 v[36:51], v[88:91], v[124:127], v[36:51]
	v_mfma_f32_32x32x16_bf16 v[36:51], v[84:87], v[128:131], v[36:51]
	ds_read_b64_tr_b16 v[116:117], v1 offset:0x600
	ds_read_b64_tr_b16 v[118:119], v1 offset:0xe00
	ds_read_b64_tr_b16 v[120:121], v1 offset:0x1600
	ds_read_b64_tr_b16 v[122:123], v1 offset:0x1e00
	ds_read_b64_tr_b16 v[124:125], v1 offset:0x2600
	ds_read_b64_tr_b16 v[126:127], v1 offset:0x2e00
	ds_read_b64_tr_b16 v[128:129], v1 offset:0x3600
	ds_read_b64_tr_b16 v[130:131], v1 offset:0x3e00
	s_waitcnt lgkmcnt(8)
	v_mfma_f32_32x32x16_bf16 v[20:35], v[96:99], v[100:103], v[20:35]
	v_mfma_f32_32x32x16_bf16 v[20:35], v[92:95], v[104:107], v[20:35]
	v_mfma_f32_32x32x16_bf16 v[20:35], v[88:91], v[108:111], v[20:35]
	v_mfma_f32_32x32x16_bf16 v[20:35], v[84:87], v[112:115], v[20:35]
	s_waitcnt lgkmcnt(0)
	v_mfma_f32_32x32x16_bf16 v[4:19], v[96:99], v[116:119], v[4:19]
	v_mfma_f32_32x32x16_bf16 v[4:19], v[92:95], v[120:123], v[4:19]
	v_mfma_f32_32x32x16_bf16 v[4:19], v[88:91], v[124:127], v[4:19]
	v_mfma_f32_32x32x16_bf16 v[4:19], v[84:87], v[128:131], v[4:19]
.LBB0_642:
	s_add_i32 s0, s4, 0xffff0000
	s_and_b32 s2, s0, 0x18000
	v_add_u32_e32 v1, s2, v185
	s_and_b64 s[12:13], s[56:57], s[62:63]
	s_cbranch_scc1 .Lqk_pre
	v_add_u32_e32 v2, v1, v234
	ds_read_b128 v[148:151], v2
	ds_read_b128 v[152:155], v2 offset:8192
	v_add_u32_e32 v2, v1, v235
	ds_read_b128 v[156:159], v2
	ds_read_b128 v[160:163], v2 offset:8192
.Lqk_pre:
	v_add_u32_e32 v2, v1, v236
	s_waitcnt lgkmcnt(0)
	v_mfma_f32_32x32x16_bf16 v[100:115], v[148:151], v[132:135], v[68:83]
	ds_read_b128 v[164:167], v2
	ds_read_b128 v[168:171], v2 offset:8192
	v_add_u32_e32 v1, v1, v237
	ds_read_b128 v[176:179], v1
	ds_read_b128 v[172:175], v1 offset:8192
	s_cmp_lt_i32 s42, s77
	s_cselect_b64 s[64:65], -1, 0
	s_cmp_ge_i32 s42, s77
	v_mfma_f32_32x32x16_bf16 v[84:99], v[152:155], v[132:135], v[68:83]
	v_mfma_f32_32x32x16_bf16 v[100:115], v[156:159], v[136:139], v[100:115]
	v_mfma_f32_32x32x16_bf16 v[84:99], v[160:163], v[136:139], v[84:99]
	s_waitcnt lgkmcnt(0)
	v_mfma_f32_32x32x16_bf16 v[100:115], v[164:167], v[140:143], v[100:115]
	s_waitcnt lgkmcnt(2)
	v_mfma_f32_32x32x16_bf16 v[84:99], v[168:171], v[140:143], v[84:99]
	s_waitcnt lgkmcnt(1)
	v_mfma_f32_32x32x16_bf16 v[100:115], v[176:179], v[144:147], v[100:115]
	s_waitcnt lgkmcnt(0)
	v_mfma_f32_32x32x16_bf16 v[84:99], v[172:175], v[144:147], v[84:99]
	s_cbranch_scc1 .LBB0_676
	v_add_u32_e32 v239, s42, v238
	v_min_i32_e32 v1, 0x9f, v239
	v_subrev_u32_e32 v1, 32, v1
	v_cmp_gt_i32_e32 vcc, 32, v239
	v_cmp_lt_i32_e64 s[0:1], -1, v239
	v_mov_b32_e32 v117, 0xf149f2ca
	v_cndmask_b32_e64 v1, v1, 0, vcc
	v_lshl_add_u32 v1, v1, 2, 0
	v_add_u32_e32 v1, 0x21000, v1
	ds_read_b32 v2, v1
	v_mov_b32_e32 v116, 0xf149f2ca
	s_and_saveexec_b64 s[10:11], s[0:1]
	s_cbranch_execz .LBB0_645
	v_min_u32_e32 v1, 0x7f, v239
	v_lshl_add_u32 v1, v1, 2, 0
	v_add_u32_e32 v1, 0x21000, v1
	ds_read_b32 v1, v1
	s_waitcnt lgkmcnt(0)
	v_add_f32_e32 v116, v100, v1
